# v2 + XCD-local group barriers narrowed from 32 workgroups to the 8 workgroups that share a row panel (independent dependency chains through G_out/w1/w2/G_in)
# speedup vs baseline: 1.0126x; 1.0073x over previous
.LBB0_60:
	s_add_u32 s0, s78, 0x200
	s_addc_u32 s1, s79, 0
	s_add_u32 s70, s78, 0x1000
	s_addc_u32 s71, s79, 0
	s_add_u32 s74, s78, 0x1100
	v_writelane_b32 v254, s0, 7
	s_addc_u32 s75, s79, 0
	s_movk_i32 s34, 0x80
	v_writelane_b32 v254, s1, 8
	s_add_u32 s0, s78, 0x1200
	s_addc_u32 s1, s79, 0
	s_add_u32 s18, s78, 0x1300
	s_addc_u32 s19, s79, 0
	v_writelane_b32 v254, s0, 9
	s_cmp_eq_u32 s2, 15
	v_mov_b32_e32 v115, 0
	v_writelane_b32 v254, s1, 10
	s_cselect_b64 s[0:1], -1, 0
	v_writelane_b32 v254, s0, 11
	s_cmp_eq_u32 s2, 14
	v_mov_b32_e32 v185, 0x358637bd
	v_writelane_b32 v254, s1, 12
	s_cselect_b64 s[0:1], -1, 0
	v_writelane_b32 v254, s0, 13
	s_cmp_eq_u32 s2, 13
	s_mov_b32 s90, 0x800000
	v_writelane_b32 v254, s1, 14
	s_cselect_b64 s[0:1], -1, 0
	v_writelane_b32 v254, s0, 15
	s_cmp_eq_u32 s2, 12
	s_movk_i32 s35, 0xc0
	v_writelane_b32 v254, s1, 16
	s_cselect_b64 s[0:1], -1, 0
	v_writelane_b32 v254, s0, 17
	s_cmp_eq_u32 s2, 11
	s_movk_i32 s72, 0x4000
	v_writelane_b32 v254, s1, 18
	s_cselect_b64 s[0:1], -1, 0
	v_writelane_b32 v254, s0, 19
	s_cmp_eq_u32 s2, 10
	s_mov_b32 s91, 0x20000
	v_writelane_b32 v254, s1, 20
	s_cselect_b64 s[0:1], -1, 0
	v_writelane_b32 v254, s0, 21
	s_cmp_eq_u32 s2, 9
	v_mov_b32_e32 v188, 0xff61b1e6
	v_writelane_b32 v254, s1, 22
	s_cselect_b64 s[0:1], -1, 0
	v_writelane_b32 v254, s0, 23
	s_cmp_eq_u32 s2, 8
	v_mov_b32_e32 v189, 0x80
	v_writelane_b32 v254, s1, 24
	s_cselect_b64 s[0:1], -1, 0
	v_writelane_b32 v254, s0, 25
	s_cmp_eq_u32 s2, 7
	v_mov_b32_e32 v190, 0xc6ea6000
	v_writelane_b32 v254, s1, 26
	s_cselect_b64 s[0:1], -1, 0
	v_writelane_b32 v254, s0, 27
	s_cmp_eq_u32 s2, 6
	v_mov_b32_e32 v191, 0xff800000
	v_writelane_b32 v254, s1, 28
	s_cselect_b64 s[0:1], -1, 0
	v_writelane_b32 v254, s0, 29
	s_cmp_eq_u32 s2, 5
	v_mov_b64_e32 v[162:163], 0x100
	v_writelane_b32 v254, s1, 30
	s_cselect_b64 s[0:1], -1, 0
	v_writelane_b32 v254, s0, 31
	s_cmp_eq_u32 s2, 4
	v_mov_b64_e32 v[164:165], 0xff
	v_writelane_b32 v254, s1, 32
	s_cselect_b64 s[0:1], -1, 0
	v_writelane_b32 v254, s0, 33
	s_cmp_eq_u32 s2, 3
	v_mov_b32_e32 v193, 0x7f61b1e6
	v_writelane_b32 v254, s1, 34
	s_cselect_b64 s[0:1], -1, 0
	v_writelane_b32 v254, s0, 35
	s_cmp_eq_u32 s2, 2
	s_movk_i32 s22, 0x1ff
	v_writelane_b32 v254, s1, 36
	s_cselect_b64 s[0:1], -1, 0
	v_writelane_b32 v254, s0, 37
	s_cmp_eq_u32 s2, 1
	s_mov_b32 s23, 0xffff0000
	v_writelane_b32 v254, s1, 38
	s_cselect_b64 s[0:1], -1, 0
	v_writelane_b32 v254, s0, 39
	s_cmp_eq_u32 s2, 0
	s_movk_i32 s73, 0x1000
	v_writelane_b32 v254, s1, 40
	s_cselect_b64 s[0:1], -1, 0
	v_writelane_b32 v254, s0, 41
	s_mov_b32 s96, 0x4138aa3b
	s_movk_i32 s97, 0x7fff
	v_writelane_b32 v254, s1, 42
	s_lshl_b32 s0, s2, 8
	s_add_u32 s0, s78, s0
	s_addc_u32 s1, s79, 0
	s_add_u32 s2, s0, 0x1400
	s_addc_u32 s3, s1, 0
	v_writelane_b32 v254, s2, 43
	s_add_u32 s0, s0, 0x2400
	s_addc_u32 s1, s1, 0
	v_writelane_b32 v254, s3, 44
	v_writelane_b32 v254, s0, 45
	s_mov_b32 s30, 0xffff
	s_movk_i32 s31, 0x5000
	v_writelane_b32 v254, s1, 46
	s_add_u32 s0, s78, 0x3400
	s_addc_u32 s1, s79, 0
	v_writelane_b32 v254, s0, 47
	s_mov_b32 s36, 0
	s_mov_b32 s25, 0
	v_writelane_b32 v254, s1, 48
	s_add_u32 s0, s78, 0x3500
	s_addc_u32 s1, s79, 0
	v_writelane_b32 v254, s0, 49
	s_brev_b32 s6, 64
	s_nop 0
	v_writelane_b32 v254, s1, 50
	s_nop 0
	v_readlane_b32 s0, v254, 0
	s_nop 3
	s_and_b32 s1, s0, 7
	s_lshl_b32 s1, s1, 10
	s_bfe_u32 s0, s0, 0x20003
	s_lshl_b32 s0, s0, 8
	s_or_b32 s0, s0, s1
	s_add_u32 s0, s82, s0
	s_addc_u32 s1, s83, 0
	s_ashr_i32 s3, s33, 31
	v_writelane_b32 v254, s0, 51
	s_cmp_lt_i32 s76, 12
	s_nop 0
	v_writelane_b32 v254, s1, 52
	s_cselect_b64 s[0:1], -1, 0
	s_cmp_gt_i32 s77, 11
	s_cselect_b64 s[4:5], -1, 0
	s_and_b64 s[0:1], s[0:1], s[4:5]
	v_writelane_b32 v254, s0, 53
	s_cmp_lt_i32 s76, 3
	s_nop 0
	v_writelane_b32 v254, s1, 54
	s_cselect_b64 s[0:1], -1, 0
	s_cmp_gt_i32 s77, 2
	s_cselect_b64 s[4:5], -1, 0
	s_and_b64 s[0:1], s[0:1], s[4:5]
	v_writelane_b32 v254, s0, 55
	s_cmpk_eq_i32 s33, 0x100
	s_nop 0
	v_writelane_b32 v254, s1, 56
	s_cselect_b64 s[0:1], -1, 0
	v_writelane_b32 v254, s0, 57
	s_cmpk_gt_i32 s33, 0xbf
	s_nop 0
	v_writelane_b32 v254, s1, 58
	s_cselect_b64 s[0:1], -1, 0
	v_writelane_b32 v254, s0, 59
	s_nop 1
	v_writelane_b32 v254, s1, 60
	s_and_b64 s[0:1], s[0:1], exec
	s_cselect_b32 s0, 0x80, 64
	s_cmp_gt_i32 s33, s0
	s_cselect_b64 s[4:5], -1, 0
	v_writelane_b32 v254, s4, 61
	s_add_i32 s2, 0, 0x14800
	s_nop 0
	v_writelane_b32 v254, s5, 62
	v_writelane_b32 v254, s0, 63
	s_sub_i32 s0, s33, s0
	s_lshl_b32 s0, s0, 3
	v_writelane_b32 v255, s0, 0
	v_readlane_b32 s0, v254, 6
	s_lshl_b32 s0, s0, 14
	s_add_i32 s0, s0, 0
	v_writelane_b32 v255, s0, 1
	s_add_i32 s0, 0, 0x20160
	v_writelane_b32 v255, s0, 2
	s_add_i32 s0, 0, 0x20164
	v_writelane_b32 v255, s0, 3
	s_add_i32 s0, 0, 0x20400
	v_writelane_b32 v255, s0, 4
	s_add_i32 s0, 0, 0x22400
	v_writelane_b32 v255, s0, 5
	s_add_i32 s0, 0, 0x15800
	v_writelane_b32 v255, s0, 6
	s_add_i32 s0, 0, 0x15000
	v_writelane_b32 v255, s0, 7
	s_add_i32 s0, 0, 0x19000
	v_writelane_b32 v255, s0, 8
	s_add_i32 s0, 0, 0x10800
	v_writelane_b32 v255, s0, 9
	s_mov_b32 s0, 0
	v_writelane_b32 v255, s0, 10
	s_mov_b64 s[0:1], 0
	v_writelane_b32 v255, s0, 11
	s_nop 1
	v_writelane_b32 v255, s1, 12
	v_writelane_b32 v255, s70, 13
	s_nop 1
	v_writelane_b32 v255, s71, 14
	v_writelane_b32 v255, s74, 15
	s_nop 1
	v_writelane_b32 v255, s75, 16
	s_branch .LBB0_64

.LBB0_126:
	s_or_b64 exec, exec, s[38:39]
	v_readlane_b32 s4, v254, 51
	v_readlane_b32 s5, v254, 52
	s_nop 4
	global_load_dword v1, v115, s[4:5] offset:2048 sc1
	s_lshl_b32 s4, s7, 3
	s_waitcnt vmcnt(0)
	v_cmp_le_u32_e32 vcc, s4, v1
	s_cbranch_vccnz .LBB0_139
	s_mov_b32 s5, 1
	s_branch .LBB0_129

.LBB0_277:
	s_or_b64 exec, exec, s[28:29]
	v_readlane_b32 s4, v254, 51
	v_readlane_b32 s5, v254, 52
	s_nop 4
	global_load_dword v1, v115, s[4:5] offset:2048 sc1
	s_lshl_b32 s4, s7, 3
	s_waitcnt vmcnt(0)
	v_cmp_le_u32_e32 vcc, s4, v1
	s_cbranch_vccnz .LBB0_290
	s_mov_b32 s5, 1
	s_branch .LBB0_280

.LBB0_1163:
	s_or_b64 exec, exec, s[10:11]
	v_readlane_b32 s8, v254, 51
	v_readlane_b32 s9, v254, 52
	v_readlane_b32 s7, v255, 10
	s_lshl_b32 s7, s7, 3
	s_nop 2
	global_load_dword v1, v115, s[8:9] offset:2048 sc1
	s_waitcnt vmcnt(0)
	v_cmp_le_u32_e32 vcc, s7, v1
	s_cbranch_vccnz .LBB0_1176
	s_mov_b32 s12, 1
	s_branch .LBB0_1166

.LBB0_1298:
	s_or_b64 exec, exec, s[8:9]
	v_readlane_b32 s4, v254, 51
	v_readlane_b32 s5, v254, 52
	s_nop 4
	global_load_dword v1, v115, s[4:5] offset:2048 sc1
	v_readlane_b32 s4, v255, 10
	s_lshl_b32 s7, s4, 3
	s_waitcnt vmcnt(0)
	v_cmp_le_u32_e32 vcc, s7, v1
	s_cbranch_vccnz .LBB0_1311
	s_mov_b32 s12, 1
	s_branch .LBB0_1301
